# micro bundle + shorter max trees (v_max3 chains without canonicalising v_max x,x): fewer VALU in per-head max phase
# speedup vs baseline: 1.0305x; 1.0049x over previous
.LBB1_19:
	v_max3_f32 v3, v26, v27, v28
	v_max3_f32 v3, v3, v29, v30
	v_max3_f32 v3, v3, v31, v32
	v_max_f32_e32 v237, v3, v33
.LBB1_20:
	v_max3_f32 v3, v1, v243, v241
	v_max3_f32 v3, v3, v242, v239
	v_max3_f32 v3, v3, v240, v237
	v_max_f32_e32 v3, v3, v238
	v_mov_b32_e32 v4, v3
	s_nop 1
	v_permlane32_swap_b32_e32 v3, v4
	v_max3_f32 v236, v3, v4, s43
	s_setprio 1
	v_sub_f32_e32 v1, v1, v236
	v_cmp_le_f32_e32 vcc, s56, v1
	s_cbranch_vccz .LBB1_82
	ds_read_b128 v[10:13], v206 offset:49152
	v_sub_f32_e32 v1, v66, v236
	v_sub_f32_e32 v3, v68, v236
	v_sub_f32_e32 v5, v70, v236
	v_sub_f32_e32 v7, v72, v236
	v_exp_f32_e32 v14, v1
	v_sub_f32_e32 v1, v67, v236
	v_exp_f32_e32 v4, v3
	v_sub_f32_e32 v3, v69, v236
	v_exp_f32_e32 v6, v5
	v_sub_f32_e32 v5, v71, v236
	v_exp_f32_e32 v8, v7
	v_sub_f32_e32 v7, v73, v236
	v_exp_f32_e32 v7, v7
	v_exp_f32_e32 v5, v5
	v_exp_f32_e32 v3, v3
	v_exp_f32_e32 v1, v1
	v_cvt_pk_f16_f32 v9, v8, v7
	v_cvt_pk_f16_f32 v8, v6, v5
	v_cvt_pk_f16_f32 v7, v4, v3
	v_cvt_pk_f16_f32 v6, v14, v1
	s_waitcnt lgkmcnt(0)
	s_nop 0
	v_mfma_f32_32x32x16_f16 v[98:113], v[10:13], v[6:9], 0
	v_mfma_f32_32x32x16_f16 v[82:97], v[194:197], v[6:9], 0
	v_sub_f32_e32 v1, v243, v236
	v_cmp_le_f32_e32 vcc, s56, v1
	s_cbranch_vccz .LBB1_23

.LBB1_46:
	v_max3_f32 v3, v26, v27, v28
	v_max3_f32 v3, v3, v29, v30
	v_max3_f32 v3, v3, v31, v32
	v_max_f32_e32 v9, v3, v33
.LBB1_47:
	v_max3_f32 v3, v1, v16, v14
	v_max3_f32 v3, v3, v15, v12
	v_max3_f32 v3, v3, v13, v9
	v_max_f32_e32 v3, v3, v11
	v_mov_b32_e32 v4, v3
	s_nop 1
	v_permlane32_swap_b32_e32 v3, v4
	v_max3_f32 v10, v236, v3, v4
	v_sub_f32_e32 v3, v236, v10
	v_exp_f32_e32 v4, v3
	s_nop 0
	v_mul_f32_e32 v82, v82, v4
	v_pk_mul_f32 v[112:113], v[4:5], v[112:113] op_sel_hi:[0,1]
	v_pk_mul_f32 v[110:111], v[4:5], v[110:111] op_sel_hi:[0,1]
	v_pk_mul_f32 v[108:109], v[4:5], v[108:109] op_sel_hi:[0,1]
	v_pk_mul_f32 v[106:107], v[4:5], v[106:107] op_sel_hi:[0,1]
	v_pk_mul_f32 v[104:105], v[4:5], v[104:105] op_sel_hi:[0,1]
	v_pk_mul_f32 v[102:103], v[4:5], v[102:103] op_sel_hi:[0,1]
	v_pk_mul_f32 v[100:101], v[4:5], v[100:101] op_sel_hi:[0,1]
	v_pk_mul_f32 v[98:99], v[4:5], v[98:99] op_sel_hi:[0,1]
	s_setprio 1
	v_sub_f32_e32 v1, v1, v10
	v_cmp_le_f32_e32 vcc, s56, v1
	s_cbranch_vccz .LBB1_86
	ds_read_b128 v[114:117], v206 offset:57344
	v_sub_f32_e32 v1, v66, v10
	v_sub_f32_e32 v3, v68, v10
	v_sub_f32_e32 v5, v70, v10
	v_sub_f32_e32 v7, v72, v10
	v_exp_f32_e32 v17, v1
	v_sub_f32_e32 v1, v67, v10
	v_exp_f32_e32 v4, v3
	v_sub_f32_e32 v3, v69, v10
	v_exp_f32_e32 v6, v5
	v_sub_f32_e32 v5, v71, v10
	v_exp_f32_e32 v8, v7
	v_sub_f32_e32 v7, v73, v10
	v_exp_f32_e32 v7, v7
	v_exp_f32_e32 v5, v5
	v_exp_f32_e32 v3, v3
	v_exp_f32_e32 v1, v1
	v_cvt_pk_f16_f32 v239, v8, v7
	v_cvt_pk_f16_f32 v238, v6, v5
	v_cvt_pk_f16_f32 v237, v4, v3
	v_cvt_pk_f16_f32 v236, v17, v1
	s_waitcnt lgkmcnt(0)
	s_nop 0
	v_mfma_f32_32x32x16_f16 v[98:113], v[114:117], v[236:239], v[98:113]
	v_mfma_f32_32x32x16_f16 v[82:97], v[194:197], v[236:239], v[82:97]
	v_sub_f32_e32 v1, v16, v10
	v_cmp_le_f32_e32 vcc, s56, v1
	s_cbranch_vccz .LBB1_50

.LBB1_64:
	v_max3_f32 v1, v66, v67, v68
	v_max3_f32 v1, v1, v69, v70
	v_max3_f32 v1, v1, v71, v72
	v_max_f32_e32 v1, v1, v73
	s_and_b64 vcc, exec, s[22:23]
	s_cbranch_vccnz .LBB1_13
.LBB1_65:
	v_max3_f32 v3, v74, v75, v76
	v_max3_f32 v3, v3, v77, v78
	v_max3_f32 v3, v3, v79, v80
	v_max_f32_e32 v243, v3, v81
	v_mov_b32_e32 v241, 0xff800000
	s_and_b64 vcc, exec, s[16:17]
	v_mov_b32_e32 v242, 0xff800000
	s_cbranch_vccnz .LBB1_14
.LBB1_66:
	v_max3_f32 v3, v50, v51, v52
	v_max3_f32 v3, v3, v53, v54
	v_max3_f32 v3, v3, v55, v56
	v_max_f32_e32 v242, v3, v57
	s_and_b64 vcc, exec, s[16:17]
	s_cbranch_vccnz .LBB1_15
.LBB1_67:
	v_max3_f32 v3, v58, v59, v60
	v_max3_f32 v3, v3, v61, v62
	v_max3_f32 v3, v3, v63, v64
	v_max_f32_e32 v241, v3, v65
	v_mov_b32_e32 v239, 0xff800000
	s_and_b64 vcc, exec, s[18:19]
	v_mov_b32_e32 v240, 0xff800000
	s_cbranch_vccnz .LBB1_16
.LBB1_68:
	v_max3_f32 v3, v34, v35, v36
	v_max3_f32 v3, v3, v37, v38
	v_max3_f32 v3, v3, v39, v40
	v_max_f32_e32 v240, v3, v41
	s_and_b64 vcc, exec, s[18:19]
	s_cbranch_vccnz .LBB1_17
.LBB1_69:
	v_max3_f32 v3, v42, v43, v44
	v_max3_f32 v3, v3, v45, v46
	v_max3_f32 v3, v3, v47, v48
	v_max_f32_e32 v239, v3, v49
	v_mov_b32_e32 v237, 0xff800000
	s_and_b64 vcc, exec, s[20:21]
	v_mov_b32_e32 v238, 0xff800000
	s_cbranch_vccnz .LBB1_18
.LBB1_70:
	v_max3_f32 v3, v18, v19, v20
	v_max3_f32 v3, v3, v21, v22
	v_max3_f32 v3, v3, v23, v24
	v_max_f32_e32 v238, v3, v25
	s_and_b64 vcc, exec, s[20:21]
	s_cbranch_vccz .LBB1_19
	s_branch .LBB1_20

.LBB1_75:
	v_max3_f32 v1, v66, v67, v68
	v_max3_f32 v1, v1, v69, v70
	v_max3_f32 v1, v1, v71, v72
	v_max_f32_e32 v1, v1, v73
	s_and_b64 vcc, exec, s[18:19]
	s_cbranch_vccnz .LBB1_40
.LBB1_76:
	v_max3_f32 v3, v74, v75, v76
	v_max3_f32 v3, v3, v77, v78
	v_max3_f32 v3, v3, v79, v80
	v_max_f32_e32 v16, v3, v81
	v_mov_b32_e32 v14, 0xff800000
	s_and_b64 vcc, exec, s[20:21]
	v_mov_b32_e32 v15, 0xff800000
	s_cbranch_vccnz .LBB1_41
.LBB1_77:
	v_max3_f32 v3, v50, v51, v52
	v_max3_f32 v3, v3, v53, v54
	v_max3_f32 v3, v3, v55, v56
	v_max_f32_e32 v15, v3, v57
	s_and_b64 vcc, exec, s[20:21]
	s_cbranch_vccnz .LBB1_42
.LBB1_78:
	v_max3_f32 v3, v58, v59, v60
	v_max3_f32 v3, v3, v61, v62
	v_max3_f32 v3, v3, v63, v64
	v_max_f32_e32 v14, v3, v65
	v_mov_b32_e32 v12, 0xff800000
	s_and_b64 vcc, exec, s[22:23]
	v_mov_b32_e32 v13, 0xff800000
	s_cbranch_vccnz .LBB1_43
.LBB1_79:
	v_max3_f32 v3, v34, v35, v36
	v_max3_f32 v3, v3, v37, v38
	v_max3_f32 v3, v3, v39, v40
	v_max_f32_e32 v13, v3, v41
	s_and_b64 vcc, exec, s[22:23]
	s_cbranch_vccnz .LBB1_44
.LBB1_80:
	v_max3_f32 v3, v42, v43, v44
	v_max3_f32 v3, v3, v45, v46
	v_max3_f32 v3, v3, v47, v48
	v_max_f32_e32 v12, v3, v49
	v_mov_b32_e32 v9, 0xff800000
	s_and_b64 vcc, exec, s[24:25]
	v_mov_b32_e32 v11, 0xff800000
	s_cbranch_vccnz .LBB1_45
.LBB1_81:
	v_max3_f32 v3, v18, v19, v20
	v_max3_f32 v3, v3, v21, v22
	v_max3_f32 v3, v3, v23, v24
	v_max_f32_e32 v11, v3, v25
	s_and_b64 vcc, exec, s[24:25]
	s_cbranch_vccz .LBB1_46
	s_branch .LBB1_47
